# L table stored half-major (gather workgroup reads 4 KB contiguous), otherwise as previous best
# baseline (speedup 1.0000x reference)
_Z6k_gemmPKfPKDv8_DF16_PDF16_S4_PK15HIP_vector_typeIiLj2EEPKiPiPS6_Pj:
	s_mov_b64 s[4:5], -1
	s_cmpk_lt_u32 s2, 0x200
	v_and_b32_e32 v1, 63, v0
	s_cbranch_scc0 .LBB1_73
	s_load_dwordx8 s[8:15], s[0:1], 0x0
	v_lshrrev_b32_e32 v145, 5, v0
	v_lshlrev_b32_e32 v4, 9, v145
	s_movk_i32 s3, 0xc3f
	v_bitop3_b32 v2, v4, s3, v0 bitop3:0xc8
	v_lshlrev_b32_e32 v132, 4, v2
	v_mov_b32_e32 v133, 0
	s_waitcnt lgkmcnt(0)
	s_mov_b64 s[24:25], s[14:15]
	v_lshl_add_u64 v[2:3], s[10:11], 0, v[132:133]
	s_movk_i32 s3, 0x1000
	v_add_co_u32_e32 v2, vcc, s3, v2
	global_load_dwordx4 v[34:37], v132, s[10:11]
	global_load_dwordx4 v[38:41], v132, s[10:11] offset:1024
	global_load_dwordx4 v[42:45], v132, s[10:11] offset:2048
	global_load_dwordx4 v[46:49], v132, s[10:11] offset:3072
	v_addc_co_u32_e32 v3, vcc, 0, v3, vcc
	global_load_dwordx4 v[50:53], v[2:3], off
	global_load_dwordx4 v[54:57], v[2:3], off offset:1024
	global_load_dwordx4 v[58:61], v[2:3], off offset:2048
	global_load_dwordx4 v[62:65], v[2:3], off offset:3072
	v_or_b32_e32 v2, v4, v1
	v_lshlrev_b32_e32 v2, 4, v2
	v_or_b32_e32 v3, 0x2000, v2
	v_or_b32_e32 v4, 0x2400, v2
	global_load_dwordx4 v[66:69], v3, s[10:11]
	global_load_dwordx4 v[70:73], v4, s[10:11]
	v_or_b32_e32 v3, 0x2800, v2
	s_lshl_b32 s3, s2, 15
	v_or_b32_e32 v4, 0x2c00, v2
	global_load_dwordx4 v[74:77], v3, s[10:11]
	global_load_dwordx4 v[78:81], v4, s[10:11]
	v_or_b32_e32 v3, 0x3000, v2
	v_or_b32_e32 v8, 0x700, v0
	s_add_u32 s4, s8, s3
	v_or_b32_e32 v4, 0x3400, v2
	global_load_dwordx4 v[82:85], v3, s[10:11]
	global_load_dwordx4 v[86:89], v4, s[10:11]
	v_or_b32_e32 v3, 0x3800, v2
	v_or_b32_e32 v2, 0x3c00, v2
	v_or_b32_e32 v6, 0x500, v0
	v_or_b32_e32 v7, 0x600, v0
	s_addc_u32 s5, s9, 0
	v_lshlrev_b32_e32 v9, 4, v8
	global_load_dwordx4 v[90:93], v3, s[10:11]
	global_load_dwordx4 v[94:97], v2, s[10:11]
	v_or_b32_e32 v5, 0x300, v0
	v_or_b32_e32 v2, 0x400, v0
	v_lshlrev_b32_e32 v10, 4, v7
	global_load_dwordx4 v[122:125], v9, s[4:5] nt
	global_load_dwordx4 v[114:117], v10, s[4:5] nt
	v_lshlrev_b32_e32 v9, 4, v6
	v_or_b32_e32 v3, 0x100, v0
	v_or_b32_e32 v4, 0x200, v0
	v_lshlrev_b32_e32 v10, 4, v2
	global_load_dwordx4 v[118:121], v9, s[4:5] nt
	global_load_dwordx4 v[106:109], v10, s[4:5] nt
	v_lshlrev_b32_e32 v9, 4, v5
	v_lshlrev_b32_e32 v10, 4, v4
	global_load_dwordx4 v[110:113], v9, s[4:5] nt
	global_load_dwordx4 v[98:101], v10, s[4:5] nt
	v_lshlrev_b32_e32 v9, 4, v3
	v_lshlrev_b32_e32 v10, 4, v0
	global_load_dwordx4 v[102:105], v9, s[4:5] nt
	global_load_dwordx4 v[126:129], v10, s[4:5] nt
	v_bfe_u32 v9, v0, 5, 1
	v_lshlrev_b32_e32 v10, 3, v0
	v_and_b32_e32 v12, 31, v0
	v_lshrrev_b32_e32 v147, 5, v4
	v_lshrrev_b32_e32 v144, 5, v5
	v_and_b32_e32 v4, 0xc0, v0
	v_lshlrev_b32_e32 v5, 3, v9
	v_and_b32_e32 v11, 0xf8, v10
	v_bfe_u32 v152, v0, 3, 2
	v_and_b32_e32 v151, 56, v10
	v_lshlrev_b32_e32 v132, 4, v12
	v_lshrrev_b32_e32 v149, 5, v3
	v_lshrrev_b32_e32 v141, 5, v6
	v_lshrrev_b32_e32 v139, 5, v7
	v_lshrrev_b32_e32 v136, 5, v8
	v_lshlrev_b32_e32 v3, 4, v9
	v_lshl_or_b32 v4, v4, 1, v5
	v_mul_u32_u24_e32 v5, 0x110, v145
	v_mul_u32_u24_e32 v6, 0x110, v12
	v_mul_u32_u24_e32 v7, 0x210, v12
	s_mov_b32 s7, 0
	v_lshl_or_b32 v137, v152, 7, v151
	v_cmp_lt_u32_e64 s[4:5], 15, v12
	v_lshl_add_u64 v[130:131], s[14:15], 0, v[132:133]
	v_mul_u32_u24_e32 v153, 0x210, v145
	v_mul_u32_u24_e32 v150, 0x210, v149
	v_mul_u32_u24_e32 v148, 0x210, v147
	v_mul_u32_u24_e32 v146, 0x210, v144
	v_or_b32_e32 v143, 32, v145
	v_mul_u32_u24_e32 v142, 0x210, v141
	v_mul_u32_u24_e32 v140, 0x210, v139
	v_mul_u32_u24_e32 v138, 0x210, v136
	s_mov_b32 s15, -1
	v_add_u32_e32 v154, v11, v5
	s_mov_b32 s3, 0x9c40
	v_lshlrev_b32_e32 v134, 4, v0
	v_lshlrev_b32_e32 v155, 4, v2
	v_add_u32_e32 v156, v3, v6
	v_add_u32_e32 v157, v4, v7
	s_mov_b32 s6, s2
.LBB1_2:
	s_waitcnt vmcnt(0)
	v_cvt_pk_f16_f32 v3, v128, v129
	v_cvt_pk_f16_f32 v2, v126, v127
	ds_write_b64 v154, v[2:3]
	v_cvt_pk_f16_f32 v3, v104, v105
	v_cvt_pk_f16_f32 v2, v102, v103
	ds_write_b64 v154, v[2:3] offset:2176
	v_cvt_pk_f16_f32 v3, v100, v101
	v_cvt_pk_f16_f32 v2, v98, v99
	ds_write_b64 v154, v[2:3] offset:4352
	v_cvt_pk_f16_f32 v3, v112, v113
	v_cvt_pk_f16_f32 v2, v110, v111
	ds_write_b64 v154, v[2:3] offset:6528
	v_cvt_pk_f16_f32 v3, v108, v109
	v_cvt_pk_f16_f32 v2, v106, v107
	ds_write_b64 v154, v[2:3] offset:8704
	v_cvt_pk_f16_f32 v3, v120, v121
	v_cvt_pk_f16_f32 v2, v118, v119
	ds_write_b64 v154, v[2:3] offset:10880
	v_cvt_pk_f16_f32 v3, v116, v117
	v_cvt_pk_f16_f32 v2, v114, v115
	s_mov_b32 s14, s6
	ds_write_b64 v154, v[2:3] offset:13056
	v_cvt_pk_f16_f32 v3, v124, v125
	v_cvt_pk_f16_f32 v2, v122, v123
	s_cmp_lt_i32 s15, 0
	ds_write_b64 v154, v[2:3] offset:15232
	s_waitcnt lgkmcnt(0)
	s_barrier
	s_cbranch_scc1 .LBB1_36
	v_add_u32_e32 v8, v137, v153
	v_add_u32_e32 v2, 0x4000, v8
	ds_read2_b64 v[2:5], v2 offset0:128 offset1:136
	s_mul_hi_u32 s18, s15, 0x68db8c
	s_mul_i32 s18, s18, 0x9c40
	v_bfe_u32 v166, v0, 3, 1
	v_mul_u32_u24_e32 v166, 0x9c40, v166
	v_add_u32_e32 v166, s18, v166
	v_and_b32_e32 v167, 7, v0
	v_lshlrev_b32_e32 v167, 4, v167
	s_lshl_b32 s6, s15, 6
	s_and_saveexec_b64 s[10:11], s[4:5]
	s_xor_b64 s[10:11], exec, s[10:11]
	s_cbranch_execz .LBB1_5
	v_or_b32_e32 v6, s6, v145
	v_add_u32_e32 v6, v6, v166
	v_lshl_or_b32 v6, v6, 7, v167
	s_waitcnt lgkmcnt(0)
	global_store_dwordx4 v6, v[2:5], s[24:25] sc1

.LBB1_7:
	s_or_b64 exec, exec, s[10:11]
	s_waitcnt lgkmcnt(0)
	v_add_u32_e32 v2, v137, v150
	v_add_u32_e32 v2, 0x4000, v2
	ds_read2_b64 v[2:5], v2 offset0:128 offset1:136
	s_and_saveexec_b64 s[10:11], s[4:5]
	s_xor_b64 s[10:11], exec, s[10:11]
	s_cbranch_execz .LBB1_9
	v_or_b32_e32 v9, s6, v149
	v_add_u32_e32 v9, v9, v166
	v_lshl_or_b32 v10, v9, 7, v167
	s_waitcnt lgkmcnt(0)
	global_store_dwordx4 v10, v[2:5], s[24:25] sc1

.LBB1_11:
	s_or_b64 exec, exec, s[10:11]
	s_waitcnt lgkmcnt(0)
	v_add_u32_e32 v2, v137, v148
	v_add_u32_e32 v2, 0x4000, v2
	ds_read2_b64 v[2:5], v2 offset0:128 offset1:136
	s_and_saveexec_b64 s[10:11], s[4:5]
	s_xor_b64 s[10:11], exec, s[10:11]
	s_cbranch_execz .LBB1_13
	v_or_b32_e32 v9, s6, v147
	v_add_u32_e32 v9, v9, v166
	v_lshl_or_b32 v10, v9, 7, v167
	s_waitcnt lgkmcnt(0)
	global_store_dwordx4 v10, v[2:5], s[24:25] sc1

.LBB1_15:
	s_or_b64 exec, exec, s[10:11]
	s_waitcnt lgkmcnt(0)
	v_add_u32_e32 v2, v137, v146
	v_add_u32_e32 v2, 0x4000, v2
	ds_read2_b64 v[2:5], v2 offset0:128 offset1:136
	s_and_saveexec_b64 s[10:11], s[4:5]
	s_xor_b64 s[10:11], exec, s[10:11]
	s_cbranch_execz .LBB1_17
	v_or_b32_e32 v9, s6, v144
	v_add_u32_e32 v9, v9, v166
	v_lshl_or_b32 v10, v9, 7, v167
	s_waitcnt lgkmcnt(0)
	global_store_dwordx4 v10, v[2:5], s[24:25] sc1

.LBB1_19:
	s_or_b64 exec, exec, s[10:11]
	s_waitcnt lgkmcnt(0)
	v_add_u32_e32 v2, 0x8000, v8
	ds_read2_b64 v[2:5], v2 offset0:192 offset1:200
	s_and_saveexec_b64 s[10:11], s[4:5]
	s_xor_b64 s[10:11], exec, s[10:11]
	s_cbranch_execz .LBB1_21
	v_or_b32_e32 v8, s6, v143
	v_add_u32_e32 v8, v8, v166
	v_lshl_or_b32 v8, v8, 7, v167
	s_waitcnt lgkmcnt(0)
	global_store_dwordx4 v8, v[2:5], s[24:25] sc1

.LBB1_23:
	s_or_b64 exec, exec, s[10:11]
	s_waitcnt lgkmcnt(0)
	v_add_u32_e32 v2, v137, v142
	v_add_u32_e32 v2, 0x4000, v2
	ds_read2_b64 v[2:5], v2 offset0:128 offset1:136
	s_and_saveexec_b64 s[10:11], s[4:5]
	s_xor_b64 s[10:11], exec, s[10:11]
	s_cbranch_execz .LBB1_25
	v_add3_u32 v8, s6, v141, v166
	v_lshl_or_b32 v8, v8, 7, v167
	s_waitcnt lgkmcnt(0)
	global_store_dwordx4 v8, v[2:5], s[24:25] sc1

.LBB1_27:
	s_or_b64 exec, exec, s[10:11]
	s_waitcnt lgkmcnt(0)
	v_add_u32_e32 v2, v137, v140
	v_add_u32_e32 v2, 0x4000, v2
	ds_read2_b64 v[2:5], v2 offset0:128 offset1:136
	s_and_saveexec_b64 s[10:11], s[4:5]
	s_xor_b64 s[10:11], exec, s[10:11]
	s_cbranch_execz .LBB1_29
	v_add3_u32 v8, s6, v139, v166
	v_lshl_or_b32 v8, v8, 7, v167
	s_waitcnt lgkmcnt(0)
	global_store_dwordx4 v8, v[2:5], s[24:25] sc1

.LBB1_31:
	s_or_b64 exec, exec, s[10:11]
	s_waitcnt lgkmcnt(0)
	v_add_u32_e32 v2, v137, v138
	v_add_u32_e32 v2, 0x4000, v2
	ds_read2_b64 v[2:5], v2 offset0:128 offset1:136
	s_and_saveexec_b64 s[10:11], s[4:5]
	s_xor_b64 s[10:11], exec, s[10:11]
	s_cbranch_execz .LBB1_33
	v_add3_u32 v6, s6, v136, v166
	v_lshl_or_b32 v6, v6, 7, v167
	s_waitcnt lgkmcnt(0)
	global_store_dwordx4 v6, v[2:5], s[24:25] sc1

.LBB1_40:
	s_mul_hi_u32 s18, s14, 0x68db8c
	s_mul_i32 s18, s18, 0x9c40
	v_bfe_u32 v166, v0, 3, 1
	v_mul_u32_u24_e32 v166, 0x9c40, v166
	v_add_u32_e32 v166, s18, v166
	v_and_b32_e32 v167, 7, v0
	v_lshlrev_b32_e32 v167, 4, v167
	s_mul_i32 s6, s14, 0xa36f
	s_lshr_b32 s6, s6, 16
	s_sub_i32 s7, s14, s6
	v_add_u32_e32 v8, v137, v153
	s_lshl_b32 s3, s14, 6
	s_bfe_u32 s7, s7, 0xf0001
	v_add_u32_e32 v2, 0x4000, v8
	s_add_i32 s7, s7, s6
	s_mul_hi_u32 s6, s3, 0x68db8bad
	ds_read2_b64 v[2:5], v2 offset0:128 offset1:136
	s_lshr_b32 s6, s6, 14
	s_mul_i32 s6, s6, 0x9c40
	s_lshr_b32 s7, s7, 8
	s_sub_i32 s6, s3, s6
	s_and_b32 s7, s7, 0xfe
	s_mov_b32 s8, 0x9c40
	v_add_u32_e32 v6, s7, v152
	v_mov_b32_e32 v7, s6
	s_and_saveexec_b64 s[6:7], s[4:5]
	s_xor_b64 s[6:7], exec, s[6:7]
	s_cbranch_execz .LBB1_42
	v_or_b32_e32 v9, s3, v145
	v_add_u32_e32 v9, v9, v166
	v_lshl_or_b32 v10, v9, 7, v167
	s_waitcnt lgkmcnt(0)
	global_store_dwordx4 v10, v[2:5], s[24:25] sc1

.LBB1_44:
	s_or_b64 exec, exec, s[6:7]
	s_waitcnt lgkmcnt(0)
	v_add_u32_e32 v2, v137, v150
	v_add_u32_e32 v2, 0x4000, v2
	ds_read2_b64 v[2:5], v2 offset0:128 offset1:136
	s_and_saveexec_b64 s[6:7], s[4:5]
	s_xor_b64 s[6:7], exec, s[6:7]
	s_cbranch_execz .LBB1_46
	v_or_b32_e32 v9, s3, v149
	v_add_u32_e32 v9, v9, v166
	v_lshl_or_b32 v10, v9, 7, v167
	s_waitcnt lgkmcnt(0)
	global_store_dwordx4 v10, v[2:5], s[24:25] sc1

.LBB1_48:
	s_or_b64 exec, exec, s[6:7]
	s_waitcnt lgkmcnt(0)
	v_add_u32_e32 v2, v137, v148
	v_add_u32_e32 v2, 0x4000, v2
	ds_read2_b64 v[2:5], v2 offset0:128 offset1:136
	s_and_saveexec_b64 s[6:7], s[4:5]
	s_xor_b64 s[6:7], exec, s[6:7]
	s_cbranch_execz .LBB1_50
	v_or_b32_e32 v9, s3, v147
	v_add_u32_e32 v9, v9, v166
	v_lshl_or_b32 v10, v9, 7, v167
	s_waitcnt lgkmcnt(0)
	global_store_dwordx4 v10, v[2:5], s[24:25] sc1

.LBB1_52:
	s_or_b64 exec, exec, s[6:7]
	s_waitcnt lgkmcnt(0)
	v_add_u32_e32 v2, v137, v146
	v_add_u32_e32 v2, 0x4000, v2
	ds_read2_b64 v[2:5], v2 offset0:128 offset1:136
	s_and_saveexec_b64 s[6:7], s[4:5]
	s_xor_b64 s[6:7], exec, s[6:7]
	s_cbranch_execz .LBB1_54
	v_or_b32_e32 v9, s3, v144
	v_add_u32_e32 v9, v9, v166
	v_lshl_or_b32 v10, v9, 7, v167
	s_waitcnt lgkmcnt(0)
	global_store_dwordx4 v10, v[2:5], s[24:25] sc1

.LBB1_56:
	s_or_b64 exec, exec, s[6:7]
	s_waitcnt lgkmcnt(0)
	v_add_u32_e32 v2, 0x8000, v8
	ds_read2_b64 v[2:5], v2 offset0:192 offset1:200
	s_and_saveexec_b64 s[6:7], s[4:5]
	s_xor_b64 s[6:7], exec, s[6:7]
	s_cbranch_execz .LBB1_58
	v_or_b32_e32 v8, s3, v143
	v_add_u32_e32 v8, v8, v166
	v_lshl_or_b32 v8, v8, 7, v167
	s_waitcnt lgkmcnt(0)
	global_store_dwordx4 v8, v[2:5], s[24:25] sc1

.LBB1_60:
	s_or_b64 exec, exec, s[6:7]
	s_waitcnt lgkmcnt(0)
	v_add_u32_e32 v2, v137, v142
	v_add_u32_e32 v2, 0x4000, v2
	ds_read2_b64 v[2:5], v2 offset0:128 offset1:136
	s_and_saveexec_b64 s[6:7], s[4:5]
	s_xor_b64 s[6:7], exec, s[6:7]
	s_cbranch_execz .LBB1_62
	v_add3_u32 v8, s3, v141, v166
	v_lshl_or_b32 v8, v8, 7, v167
	s_waitcnt lgkmcnt(0)
	global_store_dwordx4 v8, v[2:5], s[24:25] sc1

.LBB1_64:
	s_or_b64 exec, exec, s[6:7]
	s_waitcnt lgkmcnt(0)
	v_add_u32_e32 v2, v137, v140
	v_add_u32_e32 v2, 0x4000, v2
	ds_read2_b64 v[2:5], v2 offset0:128 offset1:136
	s_and_saveexec_b64 s[6:7], s[4:5]
	s_xor_b64 s[6:7], exec, s[6:7]
	s_cbranch_execz .LBB1_66
	v_add3_u32 v8, s3, v139, v166
	v_lshl_or_b32 v8, v8, 7, v167
	s_waitcnt lgkmcnt(0)
	global_store_dwordx4 v8, v[2:5], s[24:25] sc1

.LBB1_68:
	s_or_b64 exec, exec, s[6:7]
	s_waitcnt lgkmcnt(0)
	v_add_u32_e32 v2, v137, v138
	v_add_u32_e32 v2, 0x4000, v2
	ds_read2_b64 v[2:5], v2 offset0:128 offset1:136
	s_and_saveexec_b64 s[6:7], s[4:5]
	s_xor_b64 s[4:5], exec, s[6:7]
	s_cbranch_execz .LBB1_70
	v_add3_u32 v6, s3, v136, v166
	v_lshl_or_b32 v6, v6, 7, v167
	s_waitcnt lgkmcnt(0)
	global_store_dwordx4 v6, v[2:5], s[24:25] sc1

	.amdhsa_kernel _Z6k_gemmPKfPKDv8_DF16_PDF16_S4_PK15HIP_vector_typeIiLj2EEPKiPiPS6_Pj
		.amdhsa_group_segment_fixed_size 51200
		.amdhsa_private_segment_fixed_size 0
		.amdhsa_kernarg_size 72
		.amdhsa_user_sgpr_count 2
		.amdhsa_user_sgpr_dispatch_ptr 0
		.amdhsa_user_sgpr_queue_ptr 0
		.amdhsa_user_sgpr_kernarg_segment_ptr 1
		.amdhsa_user_sgpr_dispatch_id 0
		.amdhsa_user_sgpr_kernarg_preload_length 0
		.amdhsa_user_sgpr_kernarg_preload_offset 0
		.amdhsa_user_sgpr_private_segment_size 0
		.amdhsa_uses_dynamic_stack 0
		.amdhsa_enable_private_segment 0
		.amdhsa_system_sgpr_workgroup_id_x 1
		.amdhsa_system_sgpr_workgroup_id_y 0
		.amdhsa_system_sgpr_workgroup_id_z 0
		.amdhsa_system_sgpr_workgroup_info 0
		.amdhsa_system_vgpr_workitem_id 0
		.amdhsa_next_free_vgpr 168
		.amdhsa_next_free_sgpr 96
		.amdhsa_accum_offset 168
		.amdhsa_reserve_vcc 1
		.amdhsa_float_round_mode_32 0
		.amdhsa_float_round_mode_16_64 0
		.amdhsa_float_denorm_mode_32 3
		.amdhsa_float_denorm_mode_16_64 3
		.amdhsa_dx10_clamp 1
		.amdhsa_ieee_mode 1
		.amdhsa_fp16_overflow 0
		.amdhsa_tg_split 0
		.amdhsa_exception_fp_ieee_invalid_op 0
		.amdhsa_exception_fp_denorm_src 0
		.amdhsa_exception_fp_ieee_div_zero 0
		.amdhsa_exception_fp_ieee_overflow 0
		.amdhsa_exception_fp_ieee_underflow 0
		.amdhsa_exception_fp_ieee_inexact 0
		.amdhsa_exception_int_div_zero 0
	.end_amdhsa_kernel

_Z8k_gatherPK15HIP_vector_typeIiLj2EEPKjPKDv8_DF16_S7_PKfPf:
	s_lshr_b32 s3, s2, 3
	s_mul_hi_u32 s50, s3, 0xd1b71759
	s_lshr_b32 s50, s50, 10
	s_mulk_i32 s50, 0x4e2
	s_load_dwordx4 s[4:7], s[0:1], 0x0
	s_load_dwordx4 s[8:11], s[0:1], 0x10
	s_load_dwordx4 s[12:15], s[0:1], 0x20
	s_sub_i32 s3, s3, s50
	s_lshl_b32 s3, s3, 5
	s_and_b32 s51, s2, 7
	s_and_b32 s52, s2, 1
	s_lshr_b32 s53, s51, 1
	s_mul_i32 s53, s53, 0x9c40
	s_add_i32 s53, s53, s3
	v_and_b32_e32 v57, 7, v0
	v_lshrrev_b32_e32 v58, 3, v0
	v_lshlrev_b32_e32 v52, 4, v57
	v_add_u32_e32 v59, s3, v58
	v_add_u32_e32 v62, s53, v58
	v_lshl_add_u32 v63, v59, 7, v52
	v_lshlrev_b32_e32 v59, 3, v59
	v_lshl_add_u32 v54, v62, 9, v52
	s_mul_i32 s54, s51, 0x4e2000
	s_lshl_b32 s55, s52, 7
	s_lshl_b32 s56, s52, 8
	s_waitcnt lgkmcnt(0)
	global_load_dwordx2 v[60:61], v59, s[4:5]
	s_add_u32 s10, s10, s54
	s_addc_u32 s11, s11, 0
	global_load_dwordx4 v[8:11], v63, s[10:11] nt
	s_add_u32 s12, s12, s56
	s_addc_u32 s13, s13, 0
	global_load_dwordx4 v[4:7], v52, s[12:13]
	global_load_dwordx4 v[0:3], v52, s[12:13] offset:128
	s_add_u32 s14, s14, s56
	s_addc_u32 s15, s15, 0
	s_add_u32 s8, s8, s54
	s_addc_u32 s9, s9, 0
	s_mov_b32 s48, 0xffff
	v_mov_b32_e32 v56, 1.0
	s_waitcnt vmcnt(3)
	v_add_lshl_u32 v51, v60, v57, 2
	v_mov_b32_e32 v50, v61
	v_cmp_gt_i32_e32 vcc, v61, v57
	s_mov_b64 exec, vcc
	global_load_dword v49, v51, s[6:7]
	s_mov_b64 exec, -1
	s_waitcnt vmcnt(1)
	v_fma_mix_f32 v4, v8, v56, v4 op_sel_hi:[1,0,0]
	v_fma_mix_f32 v5, v8, v56, v5 op_sel:[1,0,0] op_sel_hi:[1,0,0]
	v_fma_mix_f32 v6, v9, v56, v6 op_sel_hi:[1,0,0]
	v_fma_mix_f32 v7, v9, v56, v7 op_sel:[1,0,0] op_sel_hi:[1,0,0]
	v_fma_mix_f32 v0, v10, v56, v0 op_sel_hi:[1,0,0]
	v_fma_mix_f32 v1, v10, v56, v1 op_sel:[1,0,0] op_sel_hi:[1,0,0]
	v_fma_mix_f32 v2, v11, v56, v2 op_sel_hi:[1,0,0]
	v_fma_mix_f32 v3, v11, v56, v3 op_sel:[1,0,0] op_sel_hi:[1,0,0]
	s_mov_b64 exec, -1
	s_waitcnt vmcnt(0)
	v_bfi_b32 v55, s48, v49, v48
	v_mov_b32_e32 v48, v49
	ds_swizzle_b32 v40, v55 offset:swizzle(BROADCAST,8,0)
	ds_swizzle_b32 v41, v55 offset:swizzle(BROADCAST,8,1)
	ds_swizzle_b32 v42, v55 offset:swizzle(BROADCAST,8,2)
	ds_swizzle_b32 v43, v55 offset:swizzle(BROADCAST,8,3)
	ds_swizzle_b32 v44, v55 offset:swizzle(BROADCAST,8,4)
	ds_swizzle_b32 v45, v55 offset:swizzle(BROADCAST,8,5)
	ds_swizzle_b32 v46, v55 offset:swizzle(BROADCAST,8,6)
	ds_swizzle_b32 v47, v55 offset:swizzle(BROADCAST,8,7)
	v_cmp_gt_i32_e64 s[32:33], v50, 0
	v_cmp_gt_i32_e64 s[34:35], v50, 1
	v_cmp_gt_i32_e64 s[36:37], v50, 2
	v_cmp_gt_i32_e64 s[38:39], v50, 3
	v_cmp_gt_i32_e64 s[40:41], v50, 4
	v_cmp_gt_i32_e64 s[42:43], v50, 5
	v_cmp_gt_i32_e64 s[44:45], v50, 6
	v_cmp_gt_i32_e64 s[46:47], v50, 7
	v_add_u32_e32 v50, -8, v50
	s_cmp_eq_u64 s[32:33], 0
	s_cbranch_scc1 .Lg_final
	v_cmp_gt_i32_e32 vcc, v50, v57
	v_add_u32_e32 v51, 32, v51
	s_mov_b64 exec, vcc
	global_load_dword v49, v51, s[6:7]
	s_waitcnt lgkmcnt(7)
	s_mov_b64 exec, s[32:33]
	v_and_b32_e32 v53, 0xffff, v40
	v_lshl_add_u32 v53, v53, 7, v52
	global_load_dwordx4 v[8:11], v53, s[8:9]
	s_waitcnt lgkmcnt(6)
	s_mov_b64 exec, s[34:35]
	v_and_b32_e32 v53, 0xffff, v41
	v_lshl_add_u32 v53, v53, 7, v52
	global_load_dwordx4 v[12:15], v53, s[8:9]
	s_waitcnt lgkmcnt(5)
	s_mov_b64 exec, s[36:37]
	v_and_b32_e32 v53, 0xffff, v42
	v_lshl_add_u32 v53, v53, 7, v52
	global_load_dwordx4 v[16:19], v53, s[8:9]
	s_waitcnt lgkmcnt(4)
	s_mov_b64 exec, s[38:39]
	v_and_b32_e32 v53, 0xffff, v43
	v_lshl_add_u32 v53, v53, 7, v52
	global_load_dwordx4 v[20:23], v53, s[8:9]
	s_waitcnt lgkmcnt(3)
	s_mov_b64 exec, s[40:41]
	v_and_b32_e32 v53, 0xffff, v44
	v_lshl_add_u32 v53, v53, 7, v52
	global_load_dwordx4 v[24:27], v53, s[8:9]
	s_waitcnt lgkmcnt(2)
	s_mov_b64 exec, s[42:43]
	v_and_b32_e32 v53, 0xffff, v45
	v_lshl_add_u32 v53, v53, 7, v52
	global_load_dwordx4 v[28:31], v53, s[8:9]
	s_waitcnt lgkmcnt(1)
	s_mov_b64 exec, s[44:45]
	v_and_b32_e32 v53, 0xffff, v46
	v_lshl_add_u32 v53, v53, 7, v52
	global_load_dwordx4 v[32:35], v53, s[8:9]
	s_waitcnt lgkmcnt(0)
	s_mov_b64 exec, s[46:47]
	v_and_b32_e32 v53, 0xffff, v47
	v_lshl_add_u32 v53, v53, 7, v52
	global_load_dwordx4 v[36:39], v53, s[8:9]
	s_mov_b64 s[16:17], s[32:33]
	s_mov_b64 s[18:19], s[34:35]
	s_mov_b64 s[20:21], s[36:37]
	s_mov_b64 s[22:23], s[38:39]
	s_mov_b64 s[24:25], s[40:41]
	s_mov_b64 s[26:27], s[42:43]
	s_mov_b64 s[28:29], s[44:45]
	s_mov_b64 s[30:31], s[46:47]

amdhsa.kernels:
  - .agpr_count:     0
    .args:
      - .actual_access:  read_only
        .address_space:  global
        .offset:         0
        .size:           8
        .value_kind:     global_buffer
      - .actual_access:  read_only
        .address_space:  global
        .offset:         8
        .size:           8
        .value_kind:     global_buffer
      - .actual_access:  read_only
        .address_space:  global
        .offset:         16
        .size:           8
        .value_kind:     global_buffer
      - .actual_access:  write_only
        .address_space:  global
        .offset:         24
        .size:           8
        .value_kind:     global_buffer
      - .actual_access:  write_only
        .address_space:  global
        .offset:         32
        .size:           8
        .value_kind:     global_buffer
      - .actual_access:  read_only
        .address_space:  global
        .offset:         40
        .size:           8
        .value_kind:     global_buffer
      - .actual_access:  read_only
        .address_space:  global
        .offset:         48
        .size:           8
        .value_kind:     global_buffer
      - .actual_access:  write_only
        .address_space:  global
        .offset:         56
        .size:           8
        .value_kind:     global_buffer
      - .actual_access:  read_only
        .address_space:  global
        .offset:         64
        .size:           8
        .value_kind:     global_buffer
    .group_segment_fixed_size: 27200
    .kernarg_segment_align: 8
    .kernarg_segment_size: 72
    .language:       OpenCL C
    .language_version:
      - 2
      - 0
    .max_flat_workgroup_size: 1024
    .name:           _Z6k_partPKiS0_PKfP15HIP_vector_typeIiLj2EEPiS2_S2_PDv8_DF16_S6_
    .private_segment_fixed_size: 0
    .sgpr_count:     30
    .sgpr_spill_count: 0
    .symbol:         _Z6k_partPKiS0_PKfP15HIP_vector_typeIiLj2EEPiS2_S2_PDv8_DF16_S6_.kd
    .uniform_work_group_size: 1
    .uses_dynamic_stack: false
    .vgpr_count:     30
    .vgpr_spill_count: 0
    .wavefront_size: 64
  - .agpr_count:     0
    .args:
      - .actual_access:  read_only
        .address_space:  global
        .offset:         0
        .size:           8
        .value_kind:     global_buffer
      - .actual_access:  read_only
        .address_space:  global
        .offset:         8
        .size:           8
        .value_kind:     global_buffer
      - .actual_access:  write_only
        .address_space:  global
        .offset:         16
        .size:           8
        .value_kind:     global_buffer
      - .actual_access:  write_only
        .address_space:  global
        .offset:         24
        .size:           8
        .value_kind:     global_buffer
      - .actual_access:  read_only
        .address_space:  global
        .offset:         32
        .size:           8
        .value_kind:     global_buffer
      - .actual_access:  read_only
        .address_space:  global
        .offset:         40
        .size:           8
        .value_kind:     global_buffer
      - .actual_access:  read_only
        .address_space:  global
        .offset:         48
        .size:           8
        .value_kind:     global_buffer
      - .actual_access:  write_only
        .address_space:  global
        .offset:         56
        .size:           8
        .value_kind:     global_buffer
      - .actual_access:  write_only
        .address_space:  global
        .offset:         64
        .size:           8
        .value_kind:     global_buffer
    .group_segment_fixed_size: 51200
    .kernarg_segment_align: 8
    .kernarg_segment_size: 72
    .language:       OpenCL C
    .language_version:
      - 2
      - 0
    .max_flat_workgroup_size: 256
    .name:           _Z6k_gemmPKfPKDv8_DF16_PDF16_S4_PK15HIP_vector_typeIiLj2EEPKiPiPS6_Pj
    .private_segment_fixed_size: 0
    .sgpr_count:     44
    .sgpr_spill_count: 0
    .symbol:         _Z6k_gemmPKfPKDv8_DF16_PDF16_S4_PK15HIP_vector_typeIiLj2EEPKiPiPS6_Pj.kd
    .uniform_work_group_size: 1
    .uses_dynamic_stack: false
    .vgpr_count:     168
    .vgpr_spill_count: 0
    .wavefront_size: 64
  - .agpr_count:     0
    .args:
      - .actual_access:  read_only
        .address_space:  global
        .offset:         0
        .size:           8
        .value_kind:     global_buffer
      - .actual_access:  read_only
        .address_space:  global
        .offset:         8
        .size:           8
        .value_kind:     global_buffer
      - .actual_access:  read_only
        .address_space:  global
        .offset:         16
        .size:           8
        .value_kind:     global_buffer
      - .actual_access:  read_only
        .address_space:  global
        .offset:         24
        .size:           8
        .value_kind:     global_buffer
      - .actual_access:  read_only
        .address_space:  global
        .offset:         32
        .size:           8
        .value_kind:     global_buffer
      - .actual_access:  write_only
        .address_space:  global
        .offset:         40
        .size:           8
        .value_kind:     global_buffer
    .group_segment_fixed_size: 0
    .kernarg_segment_align: 8
    .kernarg_segment_size: 48
    .language:       OpenCL C
    .language_version:
      - 2
      - 0
    .max_flat_workgroup_size: 256
    .name:           _Z8k_gatherPK15HIP_vector_typeIiLj2EEPKjPKDv8_DF16_S7_PKfPf
    .private_segment_fixed_size: 0
    .sgpr_count:     63
    .sgpr_spill_count: 0
    .symbol:         _Z8k_gatherPK15HIP_vector_typeIiLj2EEPKjPKDv8_DF16_S7_PKfPf.kd
    .uniform_work_group_size: 1
    .uses_dynamic_stack: false
    .vgpr_count:     128
    .vgpr_spill_count: 0
    .wavefront_size: 64
